# speedup vs baseline: 1.1800x; 1.0078x over previous
.LBB2_4:
	s_or_b64 exec, exec, s[6:7]
	v_lshlrev_b32_e32 v10, 2, v0
	v_and_b32_e32 v14, 12, v10
	s_movk_i32 s6, 0xf0
	v_lshlrev_b32_e32 v10, 1, v14
	v_mad_u32_u24 v20, v126, s6, v10
	s_movk_i32 s8, 0x190
	v_mov_b64_e32 v[10:11], s[14:15]
	v_mad_u64_u32 v[10:11], s[6:7], v90, s8, v[10:11]
	v_mov_b32_e32 v12, v11
	v_mad_u64_u32 v[12:13], s[6:7], v91, s8, v[12:13]
	v_mov_b32_e32 v11, v12
	v_mov_b32_e32 v121, 0
	v_lshlrev_b32_e32 v120, 2, v14
	s_and_saveexec_b64 s[6:7], vcc
	s_xor_b64 s[6:7], exec, s[6:7]
	v_mov_b32_e32 v12, 0
	v_mov_b32_e32 v13, v12
	ds_write_b64 v20, v[12:13]
	s_or_saveexec_b64 s[6:7], s[6:7]
	v_lshl_add_u64 v[10:11], v[10:11], 0, v[120:121]
	v_mov_b32_e32 v13, 0
	v_mov_b32_e32 v12, v121
	s_xor_b64 exec, exec, s[6:7]
	s_cbranch_execz .LBB2_8
	global_load_dwordx4 v[136:139], v[10:11], off
	global_load_dwordx4 v[140:143], v[10:11], off offset:64
	global_load_dwordx4 v[144:147], v[10:11], off offset:128
	global_load_dwordx4 v[148:151], v[10:11], off offset:192
	global_load_dwordx4 v[152:155], v[10:11], off offset:256
	global_load_dwordx4 v[156:159], v[10:11], off offset:320
	global_load_dwordx4 v[160:163], v[10:11], off offset:384
	s_waitcnt vmcnt(6)
	v_cvt_f16_f32_e32 v13, v136
	v_cvt_pk_f16_f32 v21, v137, v138
	v_cvt_f16_f32_e32 v23, v139
	s_waitcnt vmcnt(5)
	v_cvt_f16_f32_e32 v121, v140
	v_cvt_f16_f32_e32 v12, v141
	v_pack_b32_f16 v22, v13, v21
	v_alignbit_b32 v23, v23, v21, 16
	v_cvt_pk_f16_f32 v13, v142, v143
	ds_write_b64 v20, v[22:23]
.LBB2_8:
	s_or_b64 exec, exec, s[6:7]
	s_mov_b32 s6, 0x5040100
	v_perm_b32 v12, v12, v121, s6
	ds_write_b64 v20, v[12:13] offset:32
	s_and_saveexec_b64 s[6:7], vcc
	s_xor_b64 s[6:7], exec, s[6:7]
	v_mov_b32_e32 v12, 0
	v_mov_b32_e32 v13, v12
	ds_write_b64 v20, v[12:13] offset:64
	s_or_saveexec_b64 s[6:7], s[6:7]
	v_mov_b32_e32 v13, 0
	v_mov_b32_e32 v12, 0
	v_mov_b32_e32 v21, 0
	s_xor_b64 exec, exec, s[6:7]
	s_cbranch_execz .LBB2_12
	s_waitcnt vmcnt(4)
	v_cvt_f16_f32_e32 v13, v144
	v_cvt_pk_f16_f32 v23, v145, v146
	v_cvt_f16_f32_e32 v24, v147
	s_waitcnt vmcnt(3)
	v_cvt_f16_f32_e32 v12, v148
	v_cvt_f16_f32_e32 v21, v149
	v_pack_b32_f16 v22, v13, v23
	v_alignbit_b32 v23, v24, v23, 16
	v_cvt_pk_f16_f32 v13, v150, v151
	ds_write_b64 v20, v[22:23] offset:64
.LBB2_12:
	s_or_b64 exec, exec, s[6:7]
	s_mov_b32 s6, 0x5040100
	v_perm_b32 v12, v21, v12, s6
	ds_write_b64 v20, v[12:13] offset:96
	s_and_saveexec_b64 s[6:7], vcc
	s_xor_b64 s[6:7], exec, s[6:7]
	v_mov_b32_e32 v12, 0
	v_mov_b32_e32 v13, v12
	ds_write_b64 v20, v[12:13] offset:128
	s_or_saveexec_b64 s[6:7], s[6:7]
	v_mov_b32_e32 v13, 0
	v_mov_b32_e32 v21, 0
	v_mov_b32_e32 v12, 0
	v_mov_b32_e32 v22, 0
	s_xor_b64 exec, exec, s[6:7]
	s_cbranch_execz .LBB2_16
	s_waitcnt vmcnt(2)
	v_cvt_f16_f32_e32 v13, v152
	v_cvt_f16_f32_e32 v25, v155
	s_waitcnt vmcnt(1)
	v_cvt_f16_f32_e32 v12, v156
	v_cvt_f16_f32_e32 v22, v157
	v_cvt_pk_f16_f32 v23, v153, v154
	v_pack_b32_f16 v24, v13, v23
	v_alignbit_b32 v25, v25, v23, 16
	v_cvt_pk_f16_f32 v13, v158, v159
	ds_write_b64 v20, v[24:25] offset:128
.LBB2_16:
	s_or_b64 exec, exec, s[6:7]
	s_mov_b32 s6, 0x5040100
	v_perm_b32 v12, v22, v12, s6
	ds_write_b64 v20, v[12:13] offset:160
	v_or_b32_e32 v12, 0x60, v14
	s_movk_i32 s7, 0x64
	v_cmp_gt_u32_e32 vcc, s7, v12
	s_and_b64 s[8:9], s[4:5], vcc
	v_mov_b32_e32 v12, 0
	v_mov_b32_e32 v13, 0
	s_and_saveexec_b64 s[4:5], s[8:9]
	s_cbranch_execz .LBB2_18
	s_waitcnt vmcnt(0)
	v_cvt_f16_f32_e32 v21, v160
	v_cvt_f16_f32_e32 v12, v161
	v_cvt_pk_f16_f32 v13, v162, v163
.LBB2_18:
	s_or_b64 exec, exec, s[4:5]
	s_load_dwordx2 s[12:13], s[0:1], 0x40
	s_load_dwordx4 s[8:11], s[0:1], 0x18
	v_mov_b32_e32 v10, 0x3c00
	v_cmp_eq_u32_e64 s[0:1], 4, v14
	v_mov_b32_e32 v108, 0
	v_mov_b32_e32 v109, v108
	v_cndmask_b32_e64 v11, v21, v10, s[0:1]
	v_cndmask_b32_e64 v10, v12, v10, s[0:1]
	v_perm_b32 v12, v10, v11, s6
	s_waitcnt vmcnt(0)
	v_cmp_lt_i32_e64 s[4:5], 0, v15
	s_mov_b32 s22, 0
	v_mov_b64_e32 v[118:119], v[108:109]
	v_mov_b64_e32 v[116:117], v[108:109]
	v_mov_b64_e32 v[114:115], v[108:109]
	v_mov_b64_e32 v[112:113], v[108:109]
	v_mov_b64_e32 v[110:111], v[108:109]
	v_mov_b64_e32 v[106:107], v[108:109]
	v_mov_b64_e32 v[104:105], v[108:109]
	v_mov_b64_e32 v[102:103], v[108:109]
	v_mov_b64_e32 v[100:101], v[108:109]
	v_mov_b64_e32 v[98:99], v[108:109]
	v_mov_b64_e32 v[96:97], v[108:109]
	v_mov_b64_e32 v[94:95], v[108:109]
	v_mov_b64_e32 v[92:93], v[108:109]
	ds_write_b64 v20, v[12:13] offset:192
	s_and_saveexec_b64 s[16:17], s[4:5]
	s_cbranch_execz .LBB2_38
	v_mov_b32_e32 v121, v108
	v_mov_b32_e32 v109, v108
	v_min_i32_e32 v91, 8, v15
	v_lshl_add_u64 v[122:123], s[14:15], 0, v[120:121]
	s_mov_b64 s[18:19], 0
	s_movk_i32 s23, 0x190
	s_mov_b32 s24, 0
	v_mov_b64_e32 v[92:93], v[108:109]
	v_mov_b64_e32 v[94:95], v[108:109]
	v_mov_b64_e32 v[96:97], v[108:109]
	v_mov_b64_e32 v[98:99], v[108:109]
	v_mov_b64_e32 v[100:101], v[108:109]
	v_mov_b64_e32 v[102:103], v[108:109]
	v_mov_b64_e32 v[104:105], v[108:109]
	v_mov_b64_e32 v[106:107], v[108:109]
	v_mov_b64_e32 v[110:111], v[108:109]
	v_mov_b64_e32 v[112:113], v[108:109]
	v_mov_b64_e32 v[114:115], v[108:109]
	v_mov_b64_e32 v[116:117], v[108:109]
	v_mov_b64_e32 v[118:119], v[108:109]
	s_branch .LBB2_22
